# MoE GEMM1: epilogue table staging (slot->stats2 chain, G13/B13 vectors) requested from the K loop two/one iterations before the end instead of inside the aligned epilogue; prologue's 4-deep slot load
# speedup vs baseline: 1.0073x; 1.0073x over previous
; __device__ __forceinline__ int otid() { int t = threadIdx.x; asm volatile("" : "+v"(t)); return t; }
; #define PG8_STAGE_B(b, h, bp) PG8_STAGE2(PG8_SB(b, h), (bp) + (h) * hstepB, voffB[0], voffB[1])
; #define PG8_STAGE_A(b, h, ap, NX) do { if constexpr (GATHER) { const unsigned _o0 = (NX) ? vn[h][0] : vc[h][0], _o1 = (NX) ? vn[h][1] : vc[h][1]; PG8_STAGE2(PG8_SA(b, h), (ap), _o0, _o1); } \
;         else { PG8_STAGE2(PG8_SA(b, h), (ap) + (h) * hstepA, voffA[0], voffA[1]); } } while (0)
; #define PG8_WAIT_V(n) asm volatile("s_waitcnt vmcnt(" #n ")" ::: "memory")
; #define PG8_BAR __builtin_amdgcn_s_barrier()
; template <class Epi, class Sched, bool GATHER, bool LIGHTSKIP = false>
; __device__ __forceinline__ void gemm_phase(LAS unsigned char* lds, LAS unsigned char* xl, const int lda, const int ldb, const int K, const Sched& S, const Epi& E) {
;     ...
;     if constexpr (GATHER) { S.offsets(cur, lda, vc);
; #pragma unroll
;         for (int h = 0; h < 2; ++h) { vn[h][0] = vc[h][0]; vn[h][1] = vc[h][1]; } }
;     PG8_STAGE_B(0, 0, cB); PG8_STAGE_B(0, 1, cB); PG8_STAGE_A(0, 0, cA, false); PG8_STAGE_A(0, 1, cA, false);
;     if (wr == 1) PG8_BAR;
;     PG8_WAIT_V(2); PG8_BAR;
;     PG8_STAGE_B(1, 0, cB + kstep); PG8_STAGE_A(1, 0, cA + kstep, false); PG8_STAGE_B(1, 1, cB + kstep);
;     __device__ __forceinline__ void offsets(const GUnit& u, int lda, unsigned (&vo)[2][2]) const {
;         const int tid = otid(); int R[2], C[2];
; #pragma unroll
;         for (int i = 0; i < 2; ++i) stage_rc(tid * 16 + i * 8192, R[i], C[i]);
;         const int e = u.pm, j = u.x1 & 0xffff, n = cnt[e]; const int* slot = (const int*)(opaque_uniform(ws) + WS_SLOT);
; #pragma unroll
;         for (int h = 0; h < 2; ++h)
; #pragma unroll
;             for (int i = 0; i < 2; ++i) { const int idx = j * 256 + h * 128 + R[i]; int tok = 0; if (idx < n) tok = slot[(size_t)e * CAP + idx] >> 1;
;                 vo[h][i] = (unsigned)(tok * lda + C[i]) * 2u; }
.LBB0_1322:
	v_mov_b32_e32 v2, v0
	s_lshl_b32 s0, s28, 2
	v_ashrrev_i32_e32 v1, 31, v2
	v_lshrrev_b32_e32 v1, 26, v1
	v_lshlrev_b32_e32 v4, 4, v2
	v_add_u32_e32 v1, v2, v1
	v_bfe_i32 v2, v2, 27, 1
	v_lshrrev_b32_e32 v2, 22, v2
	v_add_u32_e32 v2, v4, v2
	v_and_b32_e32 v2, 0xfffffc00, v2
	v_sub_u32_e32 v2, v4, v2
	v_lshrrev_b32_e32 v3, 4, v2
	v_bitop3_b32 v6, v3, v2, 32 bitop3:0x6c
	v_ashrrev_i32_e32 v2, 31, v2
	v_lshrrev_b32_e32 v2, 26, v2
	s_add_i32 s0, s0, 0
	v_add_u32_e32 v2, v6, v2
	s_add_i32 s0, s0, 0x22200
	v_ashrrev_i32_e32 v7, 6, v2
	v_mov_b32_e32 v2, s0
	v_ashrrev_i32_e32 v1, 6, v1
	s_ashr_i32 s29, s28, 31
	ds_read_b32 v11, v2
	v_readfirstlane_b32 s1, v198
	v_readfirstlane_b32 s2, v199
	s_lshl_b32 s0, s55, 8
	v_lshlrev_b32_e32 v3, 3, v1
	s_and_b32 s0, s0, 0xffff00
	s_lshl_b64 s[4:5], s[28:29], 17
	v_and_b32_e32 v3, -16, v3
	s_add_u32 s1, s1, s4
	v_add_u32_e32 v8, v7, v3
	s_addc_u32 s2, s2, s5
	s_add_u32 s8, s1, 0x44a90000
	v_add_u32_e32 v2, s0, v8
	s_addc_u32 s9, s2, 0
	s_waitcnt lgkmcnt(0)
	v_cmp_lt_i32_e32 vcc, v2, v11
	v_mov_b32_e32 v241, 0
	v_mov_b32_e32 v242, 0
	v_mov_b32_e32 v243, 0
	v_mov_b32_e32 v244, 0
	v_mov_b32_e32 v9, 0
	v_ashrrev_i32_e32 v3, 31, v2
	v_mov_b32_e32 v10, 0
	s_and_saveexec_b64 s[10:11], vcc
	s_cbranch_execz .LBB0_1324
	v_lshl_add_u64 v[14:15], v[2:3], 2, s[8:9]
	global_load_dword v241, v[14:15], off
.LBB0_1324:
	s_or_b64 exec, exec, s[10:11]
	v_add_u32_e32 v4, 0x2000, v4
	v_ashrrev_i32_e32 v5, 31, v4
	v_lshrrev_b32_e32 v5, 22, v5
	v_add_u32_e32 v5, v4, v5
	v_ashrrev_i32_e32 v13, 10, v5
	v_mul_i32_i24_e32 v5, 0x400, v13
	v_sub_u32_e32 v4, v4, v5
	v_lshrrev_b32_e32 v5, 4, v4
	v_bitop3_b32 v14, v5, v4, 32 bitop3:0x6c
	v_ashrrev_i32_e32 v5, 31, v14
	v_lshrrev_b32_e32 v5, 26, v5
	v_lshlrev_b32_e32 v4, 3, v13
	v_add_u32_e32 v5, v14, v5
	v_and_b32_e32 v4, -16, v4
	v_ashrrev_i32_e32 v15, 6, v5
	v_add_u32_e32 v16, v15, v4
	v_add_u32_e32 v4, s0, v16
	v_cmp_lt_i32_e32 vcc, v4, v11
	v_ashrrev_i32_e32 v5, 31, v4
	s_and_saveexec_b64 s[10:11], vcc
	s_cbranch_execz .LBB0_1326
	v_lshl_add_u64 v[18:19], v[4:5], 2, s[8:9]
	global_load_dword v242, v[18:19], off
.LBB0_1326:
	s_or_b64 exec, exec, s[10:11]
	s_bitset1_b32 s0, 7
	v_add_u32_e32 v8, s0, v8
	v_cmp_lt_i32_e32 vcc, v8, v11
	v_mov_b32_e32 v8, 0
	v_mov_b32_e32 v17, 0
	s_and_saveexec_b64 s[10:11], vcc
	s_cbranch_execz .LBB0_1328
	v_lshl_add_u64 v[2:3], v[2:3], 2, s[8:9]
	global_load_dword v243, v[2:3], off offset:512
.LBB0_1328:
	s_or_b64 exec, exec, s[10:11]
	v_add_u32_e32 v2, s0, v16
	v_cmp_lt_i32_e32 vcc, v2, v11
	s_and_saveexec_b64 s[10:11], vcc
	s_cbranch_execz .LBB0_1330
	v_lshl_add_u64 v[2:3], v[4:5], 2, s[8:9]
	global_load_dword v244, v[2:3], off offset:512
.LBB0_1330:
	s_or_b64 exec, exec, s[10:11]
	s_waitcnt vmcnt(0) lgkmcnt(0)
	v_lshlrev_b32_e32 v241, 10, v241
	v_and_b32_e32 v10, 0xfffff800, v241
	v_lshlrev_b32_e32 v242, 10, v242
	v_and_b32_e32 v9, 0xfffff800, v242
	v_lshlrev_b32_e32 v243, 10, v243
	v_and_b32_e32 v17, 0xfffff800, v243
	v_lshlrev_b32_e32 v244, 10, v244
	v_and_b32_e32 v8, 0xfffff800, v244
	v_lshlrev_b32_e32 v1, 5, v1
	v_and_b32_e32 v2, 32, v1
	v_mul_i32_i24_e32 v1, 64, v7
	v_sub_u32_e32 v3, v6, v1
	v_mov_b32_e32 v1, 1
	v_ashrrev_i16_sdwa v3, v1, sext(v3) dst_sel:DWORD dst_unused:UNUSED_PAD src0_sel:DWORD src1_sel:BYTE_0
	v_add_u32_sdwa v2, v2, sext(v3) dst_sel:DWORD dst_unused:UNUSED_PAD src0_sel:DWORD src1_sel:WORD_0
	v_bfe_i32 v5, v12, 27, 1
	v_add_lshl_u32 v206, v17, v2, 1
	v_add_lshl_u32 v210, v10, v2, 1
	v_lshlrev_b32_e32 v2, 4, v12
	v_lshrrev_b32_e32 v5, 22, v5
	v_lshlrev_b32_e32 v4, 6, v15
	v_add_u32_e32 v5, v2, v5
	v_lshlrev_b32_e32 v3, 5, v13
	v_sub_u32_e32 v4, v14, v4
	v_and_b32_e32 v5, 0xfffffc00, v5
	v_and_b32_e32 v3, 32, v3
	v_ashrrev_i16_sdwa v4, v1, sext(v4) dst_sel:DWORD dst_unused:UNUSED_PAD src0_sel:DWORD src1_sel:BYTE_0
	v_sub_u32_e32 v5, v2, v5
	v_add_u32_sdwa v3, v3, sext(v4) dst_sel:DWORD dst_unused:UNUSED_PAD src0_sel:DWORD src1_sel:WORD_0
	v_ashrrev_i32_e32 v4, 31, v12
	v_lshrrev_b32_e32 v6, 4, v5
	v_lshrrev_b32_e32 v4, 26, v4
	v_bitop3_b32 v6, v6, v5, 32 bitop3:0x6c
	v_ashrrev_i32_e32 v5, 31, v5
	v_add_u32_e32 v4, v12, v4
	v_lshrrev_b32_e32 v5, 26, v5
	v_ashrrev_i32_e32 v4, 6, v4
	v_add_u32_e32 v5, v6, v5
	v_lshlrev_b32_e32 v7, 3, v4
	v_ashrrev_i32_e32 v5, 6, v5
	v_add_lshl_u32 v208, v9, v3, 1
	v_and_b32_e32 v7, -16, v7
	v_mul_i32_i24_e32 v9, 64, v5
	v_add_u32_e32 v7, v5, v7
	v_sub_u32_e32 v6, v6, v9
	v_lshlrev_b32_e32 v4, 5, v4
	v_ashrrev_i16_sdwa v6, v1, sext(v6) dst_sel:DWORD dst_unused:UNUSED_PAD src0_sel:DWORD src1_sel:BYTE_0
	v_lshlrev_b32_e32 v9, 1, v7
	v_lshrrev_b32_e32 v10, 2, v7
	v_and_b32_e32 v5, 3, v5
	s_mov_b32 s0, 0xfffe0
	v_and_b32_e32 v4, 32, v4
	v_bfe_i32 v6, v6, 0, 16
	v_and_b32_e32 v9, 24, v9
	v_and_b32_e32 v10, 4, v10
	v_and_or_b32 v5, v7, s0, v5
	v_or3_b32 v5, v5, v10, v9
	v_add_lshl_u32 v4, v4, v6, 1
	v_add_u32_e32 v2, 0x2000, v2
	v_lshl_add_u32 v200, v5, 12, v4
	v_ashrrev_i32_e32 v4, 31, v2
	v_lshrrev_b32_e32 v4, 22, v4
	v_add_u32_e32 v4, v2, v4
	v_ashrrev_i32_e32 v4, 10, v4
	v_mul_i32_i24_e32 v5, 0x400, v4
	v_sub_u32_e32 v2, v2, v5
	v_lshrrev_b32_e32 v5, 4, v2
	v_bitop3_b32 v2, v5, v2, 32 bitop3:0x6c
	v_ashrrev_i32_e32 v6, 31, v2
	v_lshrrev_b32_e32 v6, 26, v6
	v_lshlrev_b32_e32 v5, 3, v4
	v_add_u32_e32 v6, v2, v6
	v_and_b32_e32 v5, -16, v5
	v_ashrrev_i32_e32 v7, 6, v6
	v_add_u32_e32 v5, v7, v5
	v_and_b32_e32 v6, 0xc0, v6
	v_and_b32_e32 v7, 3, v7
	s_ashr_i32 s9, s14, 6
	v_sub_u32_e32 v2, v2, v6
	v_lshlrev_b32_e32 v6, 1, v5
	v_lshrrev_b32_e32 v9, 2, v5
	v_and_or_b32 v5, v5, s0, v7
	s_lshl_b32 s0, s9, 10
	v_lshlrev_b32_e32 v4, 5, v4
	v_ashrrev_i16_sdwa v2, v1, sext(v2) dst_sel:DWORD dst_unused:UNUSED_PAD src0_sel:DWORD src1_sel:BYTE_0
	s_add_i32 s1, s0, 0
	v_and_b32_e32 v4, 32, v4
	v_bfe_i32 v2, v2, 0, 16
	v_and_b32_e32 v6, 24, v6
	v_and_b32_e32 v9, 4, v9
	s_add_i32 m0, s1, 0x10000
	s_ashr_i32 s8, s14, 8
	v_or3_b32 v5, v5, v9, v6
	v_add_lshl_u32 v2, v4, v2, 1
	global_load_lds_dwordx4 v200, s[6:7]
	s_add_i32 m0, s1, 0x12000
	v_lshl_add_u32 v202, v5, 12, v2
	s_add_u32 s4, s6, 0x80000
	global_load_lds_dwordx4 v202, s[6:7]
	s_addc_u32 s5, s7, 0
	s_add_i32 m0, s1, 0x14000
	s_add_i32 s2, s1, 0x2000
	global_load_lds_dwordx4 v200, s[4:5]
	s_add_i32 m0, s1, 0x16000
	v_add_lshl_u32 v212, v8, v3, 1
	global_load_lds_dwordx4 v202, s[4:5]
	s_mov_b32 m0, s1
	s_add_i32 s4, s1, 0x4000
	global_load_lds_dwordx4 v210, s[30:31]
	s_mov_b32 m0, s2
	s_add_i32 s5, s1, 0x6000
	global_load_lds_dwordx4 v208, s[30:31]
	s_mov_b32 m0, s4
	v_mov_b32_e32 v3, 0
	global_load_lds_dwordx4 v206, s[30:31]
	s_mov_b32 m0, s5
	v_mov_b32_e32 v201, v3
	global_load_lds_dwordx4 v212, s[30:31]
	v_mov_b32_e32 v203, v3
	v_mov_b32_e32 v211, v3
	v_mov_b32_e32 v209, v3
	s_cmp_eq_u32 s8, 1
	v_lshl_add_u64 v[10:11], s[6:7], 0, v[200:201]
	s_mov_b32 s26, 0
	v_lshl_add_u64 v[8:9], s[6:7], 0, v[202:203]
	v_lshl_add_u64 v[4:5], s[30:31], 0, v[210:211]
	s_cselect_b64 s[10:11], -1, 0
	s_cmp_lg_u32 s8, 1
	v_lshl_add_u64 v[6:7], s[30:31], 0, v[208:209]
	s_cbranch_scc1 .LBB0_1332
	s_barrier
	s_setprio 1

; __device__ __forceinline__ int otid() { int t = threadIdx.x; asm volatile("" : "+v"(t)); return t; }
;     __device__ __forceinline__ void operator()(Acc& acc, const GUnit& u, int wr, int wc, int fr, int fq, LAS unsigned char* xl, int wid, int lane) const {
;     ...
;         { const int t = otid(), e = u.pm;
;           if (t < 256) { const int idx = (u.x1 & 0xffff) * 256 + t; int tok = 0; if (idx < cnt[e]) tok = slot[(size_t)e * CAP + idx] >> 1; tab[t] = *(const f32x2*)(stats2 + (size_t)tok * 2); }
;           else { const int cI = e * 1024 + u.pn * 256 + (t - 256); Gl[t - 256] = G13[cI]; Bl[t - 256] = B13[cI]; } }
.LBB0_1339:
	s_cmpk_eq_i32 s38, 0xe00
	s_cbranch_scc0 .Lm1ep_c_done
	v_readfirstlane_b32 s100, v198
	v_readfirstlane_b32 s101, v199
	s_and_b64 vcc, exec, s[14:15]
	s_cbranch_vccnz .Lm1ep_c_lo
	s_lshl_b32 s8, s28, 10
	s_lshl_b32 s9, s53, 8
	s_add_i32 s8, s8, s9
	v_add_u32_e32 v2, 0xffffff00, v0
	v_add_u32_e32 v4, s8, v2
	v_ashrrev_i32_e32 v5, 31, v4
	v_lshl_add_u64 v[4:5], v[4:5], 2, s[100:101]
	v_add_co_u32_e32 v134, vcc, 0x47330000, v4
	s_nop 1
	v_addc_co_u32_e32 v135, vcc, 0, v5, vcc
	global_load_dword v245, v[134:135], off
	v_add_co_u32_e32 v4, vcc, 0x47370000, v4
	s_nop 1
	v_addc_co_u32_e32 v5, vcc, 0, v5, vcc
	global_load_dword v246, v[4:5], off
	s_branch .Lm1ep_c_done
.Lm1ep_c_lo:
	s_lshl_b32 s8, s28, 2
	s_add_i32 s8, s8, 0x22200
	v_mov_b32_e32 v4, s8
	ds_read_b32 v5, v4
	s_lshl_b32 s8, s55, 8
	s_and_b32 s8, s8, 0xffff00
	v_add_u32_e32 v4, s8, v0
	v_mov_b32_e32 v245, 0
	s_mov_b32 s40, s28
	s_ashr_i32 s41, s28, 31
	s_lshl_b64 s[40:41], s[40:41], 17
	s_add_u32 s40, s100, s40
	s_addc_u32 s41, s101, s41
	s_waitcnt lgkmcnt(0)
	v_cmp_lt_i32_e32 vcc, v4, v5
	s_and_saveexec_b64 s[8:9], vcc
	v_ashrrev_i32_e32 v5, 31, v4
	v_lshl_add_u64 v[4:5], v[4:5], 2, s[40:41]
	v_add_co_u32_e32 v4, vcc, 0x44a90000, v4
	s_nop 1
	v_addc_co_u32_e32 v5, vcc, 0, v5, vcc
	global_load_dword v245, v[4:5], off
	s_or_b64 exec, exec, s[8:9]

;     __device__ __forceinline__ void operator()(Acc& acc, const GUnit& u, int wr, int wc, int fr, int fq, LAS unsigned char* xl, int wid, int lane) const {
;     ...
;           if (t < 256) { const int idx = (u.x1 & 0xffff) * 256 + t; int tok = 0; if (idx < cnt[e]) tok = slot[(size_t)e * CAP + idx] >> 1; tab[t] = *(const f32x2*)(stats2 + (size_t)tok * 2); }
.Lm1pf_done:
	s_cmpk_eq_i32 s38, 0xf00
	s_cbranch_scc0 .Lm1ep_d_done
	s_and_b64 vcc, exec, s[14:15]
	s_cbranch_vccz .Lm1ep_d_done
	v_readfirstlane_b32 s100, v198
	v_readfirstlane_b32 s101, v199
	v_ashrrev_i32_e32 v4, 1, v245
	v_ashrrev_i32_e32 v5, 31, v4
	v_lshlrev_b64 v[134:135], 1, v[4:5]
	v_lshl_add_u64 v[4:5], v[134:135], 2, s[100:101]
	v_add_co_u32_e32 v4, vcc, 0x473b0000, v4
	s_nop 1
	v_addc_co_u32_e32 v5, vcc, 0, v5, vcc
	global_load_dwordx2 v[246:247], v[4:5], off

; #define LAS __attribute__((address_space(3)))
; __device__ __forceinline__ unsigned cvt_pk_bf16(float lo, float hi) { const f32x2 v = {lo, hi}; return __builtin_bit_cast(unsigned, __builtin_convertvector(v, bf16x2_t)); }
; __device__ __forceinline__ int otid() { int t = threadIdx.x; asm volatile("" : "+v"(t)); return t; }
;     __device__ __forceinline__ void operator()(Acc& acc, const GUnit& u, int wr, int wc, int fr, int fq, LAS unsigned char* xl, int wid, int lane) const {
;     ...
;         { const int t = otid(), e = u.pm;
;           if (t < 256) { const int idx = (u.x1 & 0xffff) * 256 + t; int tok = 0; if (idx < cnt[e]) tok = slot[(size_t)e * CAP + idx] >> 1; tab[t] = *(const f32x2*)(stats2 + (size_t)tok * 2); }
;           else { const int cI = e * 1024 + u.pn * 256 + (t - 256); Gl[t - 256] = G13[cI]; Bl[t - 256] = B13[cI]; } }
;         asm volatile("s_waitcnt vmcnt(0) lgkmcnt(0)" ::: "memory"); __builtin_amdgcn_s_barrier(); asm volatile("" ::: "memory");
;         const int row0 = u.x0 * 256 + wr * 64 + fr, col0 = u.pn * 128 + wc * 32 + 8 * fq, cl = wc * 32 + 8 * fq;
; #pragma unroll
;         for (int ai = 0; ai < 2; ++ai)
; #pragma unroll
;             for (int m = 0; m < 4; ++m) { const int rl = ai * HALF + wr * 64 + m * 16 + fr; const f32x2 st = tab[rl];
;                 bf16_t* rowp = H + (size_t)(row0 + ai * HALF + m * 16) * 512 + col0;
;                 float h[8];
; #pragma unroll
;                 for (int nn = 0; nn < 2; ++nn) { const f32x4 g0 = *(const LAS f32x4*)(Gl + cl + 4 * nn), g1 = *(const LAS f32x4*)(Gl + HALF + cl + 4 * nn), b0 = *(const LAS f32x4*)(Bl + cl + 4 * nn), b1 = *(const LAS f32x4*)(Bl + HALF + cl + 4 * nn);
;                     const f32x4 a4 = (acc[ai][0][m][nn] - g0 * st.x) * st.y + b0, b4 = (acc[ai][1][m][nn] - g1 * st.x) * st.y + b1;
; #pragma unroll
;                     for (int jj = 0; jj < 4; ++jj) { const float a = a4[jj], b = b4[jj]; h[nn * 4 + jj] = a * b * __builtin_amdgcn_rcpf(1.0f + __builtin_amdgcn_exp2f(-a * 1.4426950408889634f)); } }
;                 u32x4 w; w.x = cvt_pk_bf16(h[0], h[1]); w.y = cvt_pk_bf16(h[2], h[3]); w.z = cvt_pk_bf16(h[4], h[5]); w.w = cvt_pk_bf16(h[6], h[7]);
;                 *(u32x4*)rowp = w; __builtin_amdgcn_sched_barrier(0); }
.LBB0_1355:
	v_mov_b32_e32 v2, v0
	s_waitcnt vmcnt(0)
	s_and_b64 vcc, exec, s[14:15]
	s_cbranch_vccz .Lm1ep_hi
	v_lshl_add_u32 v2, v2, 3, 0
	v_add_u32_e32 v2, 0x20000, v2
	ds_write_b64 v2, v[246:247]
	s_branch .Lm1ep_st_done
.Lm1ep_hi:
	v_add_u32_e32 v2, 0xffffff00, v2
	v_lshl_add_u32 v2, v2, 2, 0
	v_add_u32_e32 v135, 0x20800, v2
	v_add_u32_e32 v2, 0x20c00, v2
	ds_write_b32 v135, v245
	ds_write_b32 v2, v246
.Lm1ep_st_done:
	s_waitcnt vmcnt(0) lgkmcnt(0)
	s_barrier
	s_waitcnt lgkmcnt(0)
	ds_read_b64 v[168:169], v223
	ds_read_b128 v[136:139], v224
	ds_read_b128 v[140:143], v225 offset:16
	ds_read_b128 v[144:147], v226
	v_lshl_add_u32 v134, s54, 8, v209
	v_ashrrev_i32_e32 v135, 31, v134
	s_waitcnt lgkmcnt(0)
	v_pk_fma_f32 v[130:131], v[168:169], v[136:137], v[130:131] op_sel_hi:[0,1,1] neg_lo:[1,0,0] neg_hi:[1,0,0]
	v_lshlrev_b64 v[148:149], 10, v[134:135]
	v_pk_fma_f32 v[130:131], v[168:169], v[130:131], v[144:145] op_sel:[1,0,0]
	v_lshl_add_u64 v[170:171], v[204:205], 0, v[148:149]
	v_mul_f32_e32 v2, 0xbfb8aa3b, v130
	v_exp_f32_e32 v2, v2
	ds_read_b128 v[148:151], v224 offset:16
	ds_read_b128 v[152:155], v225
	ds_read_b128 v[156:159], v226 offset:16
	ds_read_b128 v[160:163], v227
	ds_read_b128 v[164:167], v227 offset:16
	v_pk_fma_f32 v[118:119], v[168:169], v[140:141], v[118:119] op_sel_hi:[0,1,1] neg_lo:[1,0,0] neg_hi:[1,0,0]
	v_add_f32_e32 v2, 1.0, v2
	v_rcp_f32_e32 v136, v2
	v_mul_f32_e32 v2, 0xbfb8aa3b, v131
	v_exp_f32_e32 v2, v2
	s_waitcnt lgkmcnt(0)
	v_pk_fma_f32 v[126:127], v[168:169], v[152:153], v[126:127] op_sel_hi:[0,1,1] neg_lo:[1,0,0] neg_hi:[1,0,0]
	v_pk_fma_f32 v[126:127], v[168:169], v[126:127], v[160:161] op_sel:[1,0,0]
	v_pk_fma_f32 v[122:123], v[168:169], v[148:149], v[122:123] op_sel_hi:[0,1,1] neg_lo:[1,0,0] neg_hi:[1,0,0]
	v_pk_mul_f32 v[126:127], v[130:131], v[126:127]
	v_pk_fma_f32 v[130:131], v[168:169], v[138:139], v[132:133] op_sel_hi:[0,1,1] neg_lo:[1,0,0] neg_hi:[1,0,0]
	v_add_f32_e32 v2, 1.0, v2
	v_pk_fma_f32 v[130:131], v[168:169], v[130:131], v[146:147] op_sel:[1,0,0]
	v_rcp_f32_e32 v137, v2
	v_mul_f32_e32 v2, 0xbfb8aa3b, v130
	v_exp_f32_e32 v2, v2
	v_mul_f32_e32 v132, 0xbfb8aa3b, v131
	v_exp_f32_e32 v133, v132
	v_pk_fma_f32 v[122:123], v[168:169], v[122:123], v[156:157] op_sel:[1,0,0]
	v_add_f32_e32 v2, 1.0, v2
	v_rcp_f32_e32 v132, v2
	v_add_f32_e32 v2, 1.0, v133
	v_rcp_f32_e32 v133, v2
	v_mul_f32_e32 v2, 0xbfb8aa3b, v122
	v_exp_f32_e32 v2, v2
	v_pk_fma_f32 v[128:129], v[168:169], v[154:155], v[128:129] op_sel_hi:[0,1,1] neg_lo:[1,0,0] neg_hi:[1,0,0]
	v_pk_fma_f32 v[128:129], v[168:169], v[128:129], v[162:163] op_sel:[1,0,0]
	v_pk_fma_f32 v[118:119], v[168:169], v[118:119], v[164:165] op_sel:[1,0,0]
	v_add_f32_e32 v2, 1.0, v2
	v_pk_mul_f32 v[128:129], v[130:131], v[128:129]
	v_rcp_f32_e32 v130, v2
	v_mul_f32_e32 v2, 0xbfb8aa3b, v123
	v_exp_f32_e32 v2, v2
	v_pk_mul_f32 v[118:119], v[122:123], v[118:119]
	v_pk_fma_f32 v[122:123], v[168:169], v[150:151], v[124:125] op_sel_hi:[0,1,1] neg_lo:[1,0,0] neg_hi:[1,0,0]
	v_pk_fma_f32 v[122:123], v[168:169], v[122:123], v[158:159] op_sel:[1,0,0]
	v_add_f32_e32 v2, 1.0, v2
	v_rcp_f32_e32 v131, v2
	v_mul_f32_e32 v2, 0xbfb8aa3b, v122
	v_exp_f32_e32 v2, v2
	v_mul_f32_e32 v124, 0xbfb8aa3b, v123
	v_pk_mul_f32 v[128:129], v[128:129], v[132:133]
	v_exp_f32_e32 v132, v124
	v_add_f32_e32 v2, 1.0, v2
	v_pk_mul_f32 v[124:125], v[118:119], v[130:131]
	v_rcp_f32_e32 v118, v2
	v_add_f32_e32 v2, 1.0, v132
	v_rcp_f32_e32 v119, v2
	v_pk_fma_f32 v[120:121], v[168:169], v[142:143], v[120:121] op_sel_hi:[0,1,1] neg_lo:[1,0,0] neg_hi:[1,0,0]
	v_lshl_or_b32 v4, s53, 7, v222
	v_pk_fma_f32 v[120:121], v[168:169], v[120:121], v[166:167] op_sel:[1,0,0]
	v_ashrrev_i32_e32 v5, 31, v4
	v_pk_mul_f32 v[120:121], v[122:123], v[120:121]
	v_pk_mul_f32 v[126:127], v[126:127], v[136:137]
	v_pk_mul_f32 v[130:131], v[120:121], v[118:119]
	v_lshlrev_b64 v[118:119], 1, v[4:5]
	v_lshl_add_u64 v[4:5], v[170:171], 0, v[118:119]
	v_cvt_pk_bf16_f32 v120, v126, v127
	v_cvt_pk_bf16_f32 v121, v128, v129
	v_cvt_pk_bf16_f32 v122, v124, v125
	v_cvt_pk_bf16_f32 v123, v130, v131
	global_store_dwordx4 v[4:5], v[120:123], off
	s_nop 1
	v_or_b32_e32 v120, 16, v134
	v_ashrrev_i32_e32 v121, 31, v120
	v_lshlrev_b64 v[132:133], 10, v[120:121]
	ds_read_b64 v[156:157], v223 offset:128
	ds_read_b128 v[120:123], v224
	ds_read_b128 v[124:127], v225 offset:16
	ds_read_b128 v[128:131], v226
	ds_read_b128 v[136:139], v224 offset:16
	ds_read_b128 v[140:143], v225
	ds_read_b128 v[144:147], v226 offset:16
	ds_read_b128 v[148:151], v227
	ds_read_b128 v[152:155], v227 offset:16
	s_waitcnt lgkmcnt(0)
; #define LAS __attribute__((address_space(3)))
; __device__ __forceinline__ unsigned cvt_pk_bf16(float lo, float hi) { const f32x2 v = {lo, hi}; return __builtin_bit_cast(unsigned, __builtin_convertvector(v, bf16x2_t)); }
;     __device__ __forceinline__ void operator()(Acc& acc, const GUnit& u, int wr, int wc, int fr, int fq, LAS unsigned char* xl, int wid, int lane) const {
;     ...
;             for (int m = 0; m < 4; ++m) { const int rl = ai * HALF + wr * 64 + m * 16 + fr; const f32x2 st = tab[rl];
;                 bf16_t* rowp = H + (size_t)(row0 + ai * HALF + m * 16) * 512 + col0;
;                 float h[8];
; #pragma unroll
;                 for (int nn = 0; nn < 2; ++nn) { const f32x4 g0 = *(const LAS f32x4*)(Gl + cl + 4 * nn), g1 = *(const LAS f32x4*)(Gl + HALF + cl + 4 * nn), b0 = *(const LAS f32x4*)(Bl + cl + 4 * nn), b1 = *(const LAS f32x4*)(Bl + HALF + cl + 4 * nn);
;                     const f32x4 a4 = (acc[ai][0][m][nn] - g0 * st.x) * st.y + b0, b4 = (acc[ai][1][m][nn] - g1 * st.x) * st.y + b1;
; #pragma unroll
;                     for (int jj = 0; jj < 4; ++jj) { const float a = a4[jj], b = b4[jj]; h[nn * 4 + jj] = a * b * __builtin_amdgcn_rcpf(1.0f + __builtin_amdgcn_exp2f(-a * 1.4426950408889634f)); } }
;                 u32x4 w; w.x = cvt_pk_bf16(h[0], h[1]); w.y = cvt_pk_bf16(h[2], h[3]); w.z = cvt_pk_bf16(h[4], h[5]); w.w = cvt_pk_bf16(h[6], h[7]);
;                 *(u32x4*)rowp = w; __builtin_amdgcn_sched_barrier(0); }
	v_pk_fma_f32 v[114:115], v[156:157], v[120:121], v[114:115] op_sel_hi:[0,1,1] neg_lo:[1,0,0] neg_hi:[1,0,0]
	v_pk_fma_f32 v[102:103], v[156:157], v[124:125], v[102:103] op_sel_hi:[0,1,1] neg_lo:[1,0,0] neg_hi:[1,0,0]
	v_pk_fma_f32 v[114:115], v[156:157], v[114:115], v[128:129] op_sel:[1,0,0]
	v_pk_fma_f32 v[110:111], v[156:157], v[140:141], v[110:111] op_sel_hi:[0,1,1] neg_lo:[1,0,0] neg_hi:[1,0,0]
	v_mul_f32_e32 v2, 0xbfb8aa3b, v114
	v_exp_f32_e32 v2, v2
	v_pk_fma_f32 v[110:111], v[156:157], v[110:111], v[148:149] op_sel:[1,0,0]
	v_pk_fma_f32 v[106:107], v[156:157], v[136:137], v[106:107] op_sel_hi:[0,1,1] neg_lo:[1,0,0] neg_hi:[1,0,0]
	v_pk_mul_f32 v[110:111], v[114:115], v[110:111]
	v_add_f32_e32 v2, 1.0, v2
	v_rcp_f32_e32 v120, v2
	v_mul_f32_e32 v2, 0xbfb8aa3b, v115
	v_exp_f32_e32 v2, v2
	v_pk_fma_f32 v[114:115], v[156:157], v[122:123], v[116:117] op_sel_hi:[0,1,1] neg_lo:[1,0,0] neg_hi:[1,0,0]
	v_pk_fma_f32 v[114:115], v[156:157], v[114:115], v[130:131] op_sel:[1,0,0]
	v_pk_fma_f32 v[106:107], v[156:157], v[106:107], v[144:145] op_sel:[1,0,0]
	v_add_f32_e32 v2, 1.0, v2
	v_rcp_f32_e32 v121, v2
	v_mul_f32_e32 v2, 0xbfb8aa3b, v114
	v_exp_f32_e32 v2, v2
	v_mul_f32_e32 v116, 0xbfb8aa3b, v115
	v_exp_f32_e32 v117, v116
	v_pk_fma_f32 v[112:113], v[156:157], v[142:143], v[112:113] op_sel_hi:[0,1,1] neg_lo:[1,0,0] neg_hi:[1,0,0]
	v_add_f32_e32 v2, 1.0, v2
	v_rcp_f32_e32 v116, v2
	v_add_f32_e32 v2, 1.0, v117
	v_rcp_f32_e32 v117, v2
	v_mul_f32_e32 v2, 0xbfb8aa3b, v106
	v_exp_f32_e32 v2, v2
	v_pk_fma_f32 v[112:113], v[156:157], v[112:113], v[150:151] op_sel:[1,0,0]
	v_pk_fma_f32 v[102:103], v[156:157], v[102:103], v[152:153] op_sel:[1,0,0]
	v_pk_mul_f32 v[112:113], v[114:115], v[112:113]
	v_add_f32_e32 v2, 1.0, v2
	v_rcp_f32_e32 v114, v2
	v_mul_f32_e32 v2, 0xbfb8aa3b, v107
	v_exp_f32_e32 v2, v2
	v_pk_mul_f32 v[102:103], v[106:107], v[102:103]
	v_pk_fma_f32 v[106:107], v[156:157], v[138:139], v[108:109] op_sel_hi:[0,1,1] neg_lo:[1,0,0] neg_hi:[1,0,0]
	v_pk_fma_f32 v[106:107], v[156:157], v[106:107], v[146:147] op_sel:[1,0,0]
	v_add_f32_e32 v2, 1.0, v2
	v_rcp_f32_e32 v115, v2
	v_mul_f32_e32 v2, 0xbfb8aa3b, v106
	v_exp_f32_e32 v2, v2
	v_mul_f32_e32 v108, 0xbfb8aa3b, v107
	v_pk_mul_f32 v[112:113], v[112:113], v[116:117]
	v_exp_f32_e32 v116, v108
	v_add_f32_e32 v2, 1.0, v2
	v_pk_mul_f32 v[108:109], v[102:103], v[114:115]
	v_rcp_f32_e32 v102, v2
	v_add_f32_e32 v2, 1.0, v116
	v_rcp_f32_e32 v103, v2
	v_pk_fma_f32 v[104:105], v[156:157], v[126:127], v[104:105] op_sel_hi:[0,1,1] neg_lo:[1,0,0] neg_hi:[1,0,0]
	v_pk_fma_f32 v[104:105], v[156:157], v[104:105], v[154:155] op_sel:[1,0,0]
	v_lshl_add_u64 v[132:133], v[204:205], 0, v[132:133]
	v_pk_mul_f32 v[104:105], v[106:107], v[104:105]
	v_pk_mul_f32 v[110:111], v[110:111], v[120:121]
	v_pk_mul_f32 v[106:107], v[104:105], v[102:103]
	v_lshl_add_u64 v[114:115], v[132:133], 0, v[118:119]
	v_cvt_pk_bf16_f32 v102, v110, v111
	v_cvt_pk_bf16_f32 v103, v112, v113
	v_cvt_pk_bf16_f32 v104, v108, v109
	v_cvt_pk_bf16_f32 v105, v106, v107
	global_store_dwordx4 v[114:115], v[102:105], off
	s_nop 1
	v_or_b32_e32 v102, 32, v134
	v_ashrrev_i32_e32 v103, 31, v102
	v_lshlrev_b64 v[114:115], 10, v[102:103]
	ds_read_b64 v[132:133], v223 offset:256
	ds_read_b128 v[102:105], v224
	ds_read_b128 v[106:109], v225 offset:16
	ds_read_b128 v[110:113], v226
	v_lshl_add_u64 v[140:141], v[204:205], 0, v[114:115]
	ds_read_b128 v[114:117], v224 offset:16
	ds_read_b128 v[120:123], v225
	s_waitcnt lgkmcnt(0)
	v_pk_fma_f32 v[98:99], v[132:133], v[102:103], v[98:99] op_sel_hi:[0,1,1] neg_lo:[1,0,0] neg_hi:[1,0,0]
	ds_read_b128 v[124:127], v226 offset:16
	ds_read_b128 v[128:131], v227
	ds_read_b128 v[136:139], v227 offset:16
	v_pk_fma_f32 v[98:99], v[132:133], v[98:99], v[110:111] op_sel:[1,0,0]
	v_pk_fma_f32 v[90:91], v[132:133], v[114:115], v[90:91] op_sel_hi:[0,1,1] neg_lo:[1,0,0] neg_hi:[1,0,0]
	v_mul_f32_e32 v2, 0xbfb8aa3b, v98
	v_exp_f32_e32 v2, v2
	v_pk_fma_f32 v[94:95], v[132:133], v[120:121], v[94:95] op_sel_hi:[0,1,1] neg_lo:[1,0,0] neg_hi:[1,0,0]
	s_waitcnt lgkmcnt(0)
	v_pk_fma_f32 v[94:95], v[132:133], v[94:95], v[128:129] op_sel:[1,0,0]
	v_pk_fma_f32 v[90:91], v[132:133], v[90:91], v[124:125] op_sel:[1,0,0]
	v_add_f32_e32 v2, 1.0, v2
	v_rcp_f32_e32 v102, v2
	v_mul_f32_e32 v2, 0xbfb8aa3b, v99
	v_exp_f32_e32 v2, v2
	v_pk_mul_f32 v[94:95], v[98:99], v[94:95]
	v_pk_fma_f32 v[98:99], v[132:133], v[104:105], v[100:101] op_sel_hi:[0,1,1] neg_lo:[1,0,0] neg_hi:[1,0,0]
	v_pk_fma_f32 v[98:99], v[132:133], v[98:99], v[112:113] op_sel:[1,0,0]
	v_add_f32_e32 v2, 1.0, v2
	v_rcp_f32_e32 v103, v2
	v_mul_f32_e32 v2, 0xbfb8aa3b, v98
	v_exp_f32_e32 v2, v2
	v_mul_f32_e32 v100, 0xbfb8aa3b, v99
	v_exp_f32_e32 v101, v100
	v_pk_fma_f32 v[96:97], v[132:133], v[122:123], v[96:97] op_sel_hi:[0,1,1] neg_lo:[1,0,0] neg_hi:[1,0,0]
	v_add_f32_e32 v2, 1.0, v2
	v_rcp_f32_e32 v100, v2
	v_add_f32_e32 v2, 1.0, v101
	v_rcp_f32_e32 v101, v2
	v_mul_f32_e32 v2, 0xbfb8aa3b, v90
	v_exp_f32_e32 v2, v2
	v_pk_fma_f32 v[96:97], v[132:133], v[96:97], v[130:131] op_sel:[1,0,0]
	v_pk_fma_f32 v[86:87], v[132:133], v[106:107], v[86:87] op_sel_hi:[0,1,1] neg_lo:[1,0,0] neg_hi:[1,0,0]
	v_pk_mul_f32 v[96:97], v[98:99], v[96:97]
	v_add_f32_e32 v2, 1.0, v2
	v_rcp_f32_e32 v98, v2
	v_mul_f32_e32 v2, 0xbfb8aa3b, v91
	v_exp_f32_e32 v2, v2
	v_pk_fma_f32 v[86:87], v[132:133], v[86:87], v[136:137] op_sel:[1,0,0]
	v_pk_mul_f32 v[96:97], v[96:97], v[100:101]
	v_pk_mul_f32 v[86:87], v[90:91], v[86:87]
	v_pk_fma_f32 v[90:91], v[132:133], v[116:117], v[92:93] op_sel_hi:[0,1,1] neg_lo:[1,0,0] neg_hi:[1,0,0]
	v_add_f32_e32 v2, 1.0, v2
	v_pk_fma_f32 v[90:91], v[132:133], v[90:91], v[126:127] op_sel:[1,0,0]
	v_rcp_f32_e32 v99, v2
	v_mul_f32_e32 v2, 0xbfb8aa3b, v90
	v_exp_f32_e32 v2, v2
	v_mul_f32_e32 v92, 0xbfb8aa3b, v91
	v_exp_f32_e32 v100, v92
	v_pk_mul_f32 v[92:93], v[86:87], v[98:99]
	v_add_f32_e32 v2, 1.0, v2
	v_rcp_f32_e32 v86, v2
	v_add_f32_e32 v2, 1.0, v100
	v_rcp_f32_e32 v87, v2
	v_pk_fma_f32 v[88:89], v[132:133], v[108:109], v[88:89] op_sel_hi:[0,1,1] neg_lo:[1,0,0] neg_hi:[1,0,0]
	v_pk_fma_f32 v[88:89], v[132:133], v[88:89], v[138:139] op_sel:[1,0,0]
	v_pk_mul_f32 v[94:95], v[94:95], v[102:103]
	v_pk_mul_f32 v[88:89], v[90:91], v[88:89]
	v_lshl_add_u64 v[98:99], v[140:141], 0, v[118:119]
	v_pk_mul_f32 v[90:91], v[88:89], v[86:87]
	v_cvt_pk_bf16_f32 v86, v94, v95
	v_cvt_pk_bf16_f32 v87, v96, v97
	v_cvt_pk_bf16_f32 v88, v92, v93
	v_cvt_pk_bf16_f32 v89, v90, v91
	global_store_dwordx4 v[98:99], v[86:89], off
	s_nop 1
	v_or_b32_e32 v86, 48, v134
	v_ashrrev_i32_e32 v87, 31, v86
	v_lshlrev_b64 v[98:99], 10, v[86:87]
	ds_read_b64 v[120:121], v223 offset:384
	ds_read_b128 v[86:89], v224
	ds_read_b128 v[90:93], v225 offset:16
	ds_read_b128 v[94:97], v226
	v_lshl_add_u64 v[122:123], v[204:205], 0, v[98:99]
	ds_read_b128 v[98:101], v224 offset:16
	ds_read_b128 v[102:105], v225
	s_waitcnt lgkmcnt(0)
; #define LAS __attribute__((address_space(3)))
; __device__ __forceinline__ unsigned cvt_pk_bf16(float lo, float hi) { const f32x2 v = {lo, hi}; return __builtin_bit_cast(unsigned, __builtin_convertvector(v, bf16x2_t)); }
;     __device__ __forceinline__ void operator()(Acc& acc, const GUnit& u, int wr, int wc, int fr, int fq, LAS unsigned char* xl, int wid, int lane) const {
;     ...
;             for (int m = 0; m < 4; ++m) { const int rl = ai * HALF + wr * 64 + m * 16 + fr; const f32x2 st = tab[rl];
;                 bf16_t* rowp = H + (size_t)(row0 + ai * HALF + m * 16) * 512 + col0;
;                 float h[8];
; #pragma unroll
;                 for (int nn = 0; nn < 2; ++nn) { const f32x4 g0 = *(const LAS f32x4*)(Gl + cl + 4 * nn), g1 = *(const LAS f32x4*)(Gl + HALF + cl + 4 * nn), b0 = *(const LAS f32x4*)(Bl + cl + 4 * nn), b1 = *(const LAS f32x4*)(Bl + HALF + cl + 4 * nn);
;                     const f32x4 a4 = (acc[ai][0][m][nn] - g0 * st.x) * st.y + b0, b4 = (acc[ai][1][m][nn] - g1 * st.x) * st.y + b1;
; #pragma unroll
;                     for (int jj = 0; jj < 4; ++jj) { const float a = a4[jj], b = b4[jj]; h[nn * 4 + jj] = a * b * __builtin_amdgcn_rcpf(1.0f + __builtin_amdgcn_exp2f(-a * 1.4426950408889634f)); } }
;                 u32x4 w; w.x = cvt_pk_bf16(h[0], h[1]); w.y = cvt_pk_bf16(h[2], h[3]); w.z = cvt_pk_bf16(h[4], h[5]); w.w = cvt_pk_bf16(h[6], h[7]);
;                 *(u32x4*)rowp = w; __builtin_amdgcn_sched_barrier(0); }
	v_pk_fma_f32 v[82:83], v[120:121], v[86:87], v[82:83] op_sel_hi:[0,1,1] neg_lo:[1,0,0] neg_hi:[1,0,0]
	ds_read_b128 v[106:109], v226 offset:16
	ds_read_b128 v[110:113], v227
	ds_read_b128 v[114:117], v227 offset:16
	v_pk_fma_f32 v[82:83], v[120:121], v[82:83], v[94:95] op_sel:[1,0,0]
	v_pk_fma_f32 v[74:75], v[120:121], v[98:99], v[74:75] op_sel_hi:[0,1,1] neg_lo:[1,0,0] neg_hi:[1,0,0]
	v_mul_f32_e32 v2, 0xbfb8aa3b, v82
	v_exp_f32_e32 v2, v2
	v_pk_fma_f32 v[78:79], v[120:121], v[102:103], v[78:79] op_sel_hi:[0,1,1] neg_lo:[1,0,0] neg_hi:[1,0,0]
	s_waitcnt lgkmcnt(0)
	v_pk_fma_f32 v[78:79], v[120:121], v[78:79], v[110:111] op_sel:[1,0,0]
	v_pk_fma_f32 v[74:75], v[120:121], v[74:75], v[106:107] op_sel:[1,0,0]
	v_add_f32_e32 v2, 1.0, v2
	v_rcp_f32_e32 v86, v2
	v_mul_f32_e32 v2, 0xbfb8aa3b, v83
	v_exp_f32_e32 v2, v2
	v_pk_mul_f32 v[78:79], v[82:83], v[78:79]
	v_pk_fma_f32 v[82:83], v[120:121], v[88:89], v[84:85] op_sel_hi:[0,1,1] neg_lo:[1,0,0] neg_hi:[1,0,0]
	v_pk_fma_f32 v[82:83], v[120:121], v[82:83], v[96:97] op_sel:[1,0,0]
	v_add_f32_e32 v2, 1.0, v2
	v_rcp_f32_e32 v87, v2
	v_mul_f32_e32 v2, 0xbfb8aa3b, v82
	v_exp_f32_e32 v2, v2
	v_mul_f32_e32 v84, 0xbfb8aa3b, v83
	v_exp_f32_e32 v85, v84
	v_pk_fma_f32 v[80:81], v[120:121], v[104:105], v[80:81] op_sel_hi:[0,1,1] neg_lo:[1,0,0] neg_hi:[1,0,0]
	v_add_f32_e32 v2, 1.0, v2
	v_rcp_f32_e32 v84, v2
	v_add_f32_e32 v2, 1.0, v85
	v_rcp_f32_e32 v85, v2
	v_mul_f32_e32 v2, 0xbfb8aa3b, v74
	v_exp_f32_e32 v2, v2
	v_pk_fma_f32 v[80:81], v[120:121], v[80:81], v[112:113] op_sel:[1,0,0]
	v_pk_fma_f32 v[70:71], v[120:121], v[90:91], v[70:71] op_sel_hi:[0,1,1] neg_lo:[1,0,0] neg_hi:[1,0,0]
	v_pk_mul_f32 v[80:81], v[82:83], v[80:81]
	v_add_f32_e32 v2, 1.0, v2
	v_rcp_f32_e32 v82, v2
	v_mul_f32_e32 v2, 0xbfb8aa3b, v75
	v_exp_f32_e32 v2, v2
	v_pk_fma_f32 v[70:71], v[120:121], v[70:71], v[114:115] op_sel:[1,0,0]
	v_pk_mul_f32 v[80:81], v[80:81], v[84:85]
	v_pk_mul_f32 v[70:71], v[74:75], v[70:71]
	v_pk_fma_f32 v[74:75], v[120:121], v[100:101], v[76:77] op_sel_hi:[0,1,1] neg_lo:[1,0,0] neg_hi:[1,0,0]
	v_add_f32_e32 v2, 1.0, v2
	v_pk_fma_f32 v[74:75], v[120:121], v[74:75], v[108:109] op_sel:[1,0,0]
	v_rcp_f32_e32 v83, v2
	v_mul_f32_e32 v2, 0xbfb8aa3b, v74
	v_exp_f32_e32 v2, v2
	v_mul_f32_e32 v76, 0xbfb8aa3b, v75
	v_exp_f32_e32 v84, v76
	v_pk_mul_f32 v[76:77], v[70:71], v[82:83]
	v_add_f32_e32 v2, 1.0, v2
	v_rcp_f32_e32 v70, v2
	v_add_f32_e32 v2, 1.0, v84
	v_rcp_f32_e32 v71, v2
	v_pk_fma_f32 v[72:73], v[120:121], v[92:93], v[72:73] op_sel_hi:[0,1,1] neg_lo:[1,0,0] neg_hi:[1,0,0]
	v_pk_fma_f32 v[72:73], v[120:121], v[72:73], v[116:117] op_sel:[1,0,0]
	v_pk_mul_f32 v[78:79], v[78:79], v[86:87]
	v_pk_mul_f32 v[72:73], v[74:75], v[72:73]
	v_lshl_add_u64 v[82:83], v[122:123], 0, v[118:119]
	v_pk_mul_f32 v[74:75], v[72:73], v[70:71]
	v_cvt_pk_bf16_f32 v70, v78, v79
	v_cvt_pk_bf16_f32 v71, v80, v81
	v_cvt_pk_bf16_f32 v72, v76, v77
	v_cvt_pk_bf16_f32 v73, v74, v75
	global_store_dwordx4 v[82:83], v[70:73], off
	ds_read_b64 v[102:103], v223 offset:1024
	ds_read_b128 v[70:73], v224
	ds_read_b128 v[74:77], v226
	ds_read_b128 v[78:81], v225 offset:16
	ds_read_b128 v[82:85], v224 offset:16
	ds_read_b128 v[86:89], v225
	s_waitcnt lgkmcnt(0)
	v_pk_fma_f32 v[66:67], v[102:103], v[70:71], v[66:67] op_sel_hi:[0,1,1] neg_lo:[1,0,0] neg_hi:[1,0,0]
	v_pk_fma_f32 v[66:67], v[102:103], v[66:67], v[74:75] op_sel:[1,0,0]
	ds_read_b128 v[90:93], v226 offset:16
	ds_read_b128 v[94:97], v227
	ds_read_b128 v[98:101], v227 offset:16
	v_mul_f32_e32 v2, 0xbfb8aa3b, v66
	v_exp_f32_e32 v2, v2
	v_pk_fma_f32 v[62:63], v[102:103], v[86:87], v[62:63] op_sel_hi:[0,1,1] neg_lo:[1,0,0] neg_hi:[1,0,0]
	s_waitcnt lgkmcnt(0)
	v_pk_fma_f32 v[62:63], v[102:103], v[62:63], v[94:95] op_sel:[1,0,0]
	v_pk_fma_f32 v[58:59], v[102:103], v[82:83], v[58:59] op_sel_hi:[0,1,1] neg_lo:[1,0,0] neg_hi:[1,0,0]
	v_add_f32_e32 v2, 1.0, v2
	v_rcp_f32_e32 v70, v2
	v_mul_f32_e32 v2, 0xbfb8aa3b, v67
	v_exp_f32_e32 v2, v2
	v_pk_mul_f32 v[62:63], v[66:67], v[62:63]
	v_pk_fma_f32 v[66:67], v[102:103], v[72:73], v[68:69] op_sel_hi:[0,1,1] neg_lo:[1,0,0] neg_hi:[1,0,0]
	v_pk_fma_f32 v[66:67], v[102:103], v[66:67], v[76:77] op_sel:[1,0,0]
	v_add_f32_e32 v2, 1.0, v2
	v_rcp_f32_e32 v71, v2
	v_mul_f32_e32 v2, 0xbfb8aa3b, v66
	v_exp_f32_e32 v2, v2
	v_mul_f32_e32 v68, 0xbfb8aa3b, v67
	v_exp_f32_e32 v69, v68
	v_pk_fma_f32 v[58:59], v[102:103], v[58:59], v[90:91] op_sel:[1,0,0]
	v_add_f32_e32 v2, 1.0, v2
	v_rcp_f32_e32 v68, v2
	v_add_f32_e32 v2, 1.0, v69
	v_rcp_f32_e32 v69, v2
	v_mul_f32_e32 v2, 0xbfb8aa3b, v58
	v_exp_f32_e32 v2, v2
	v_pk_fma_f32 v[64:65], v[102:103], v[88:89], v[64:65] op_sel_hi:[0,1,1] neg_lo:[1,0,0] neg_hi:[1,0,0]
	v_pk_fma_f32 v[64:65], v[102:103], v[64:65], v[96:97] op_sel:[1,0,0]
	v_pk_fma_f32 v[54:55], v[102:103], v[78:79], v[54:55] op_sel_hi:[0,1,1] neg_lo:[1,0,0] neg_hi:[1,0,0]
	v_add_f32_e32 v2, 1.0, v2
	v_pk_mul_f32 v[64:65], v[66:67], v[64:65]
	v_rcp_f32_e32 v66, v2
	v_mul_f32_e32 v2, 0xbfb8aa3b, v59
	v_exp_f32_e32 v2, v2
	v_pk_fma_f32 v[54:55], v[102:103], v[54:55], v[98:99] op_sel:[1,0,0]
	v_pk_mul_f32 v[64:65], v[64:65], v[68:69]
	v_pk_mul_f32 v[54:55], v[58:59], v[54:55]
	v_pk_fma_f32 v[58:59], v[102:103], v[84:85], v[60:61] op_sel_hi:[0,1,1] neg_lo:[1,0,0] neg_hi:[1,0,0]
	v_add_f32_e32 v2, 1.0, v2
	v_pk_fma_f32 v[58:59], v[102:103], v[58:59], v[92:93] op_sel:[1,0,0]
	v_rcp_f32_e32 v67, v2
	v_mul_f32_e32 v2, 0xbfb8aa3b, v58
	v_exp_f32_e32 v2, v2
	v_mul_f32_e32 v60, 0xbfb8aa3b, v59
	v_exp_f32_e32 v68, v60
	v_pk_mul_f32 v[60:61], v[54:55], v[66:67]
	v_add_f32_e32 v2, 1.0, v2
	v_rcp_f32_e32 v54, v2
	v_add_f32_e32 v2, 1.0, v68
	v_rcp_f32_e32 v55, v2
	v_pk_fma_f32 v[56:57], v[102:103], v[80:81], v[56:57] op_sel_hi:[0,1,1] neg_lo:[1,0,0] neg_hi:[1,0,0]
	v_pk_fma_f32 v[56:57], v[102:103], v[56:57], v[100:101] op_sel:[1,0,0]
	v_pk_mul_f32 v[62:63], v[62:63], v[70:71]
	v_pk_mul_f32 v[56:57], v[58:59], v[56:57]
	s_nop 0
	v_pk_mul_f32 v[58:59], v[56:57], v[54:55]
	v_cvt_pk_bf16_f32 v54, v62, v63
	v_cvt_pk_bf16_f32 v57, v58, v59
	v_add_co_u32_e32 v58, vcc, s44, v4
	v_cvt_pk_bf16_f32 v55, v64, v65
	v_cvt_pk_bf16_f32 v56, v60, v61
	v_addc_co_u32_e32 v59, vcc, 0, v5, vcc
	global_store_dwordx4 v[58:59], v[54:57], off
	ds_read_b64 v[86:87], v223 offset:1152
	ds_read_b128 v[54:57], v224
	ds_read_b128 v[58:61], v226
	ds_read_b128 v[62:65], v225 offset:16
	ds_read_b128 v[66:69], v224 offset:16
	ds_read_b128 v[70:73], v225
	s_waitcnt lgkmcnt(0)
; #define LAS __attribute__((address_space(3)))
; __device__ __forceinline__ unsigned cvt_pk_bf16(float lo, float hi) { const f32x2 v = {lo, hi}; return __builtin_bit_cast(unsigned, __builtin_convertvector(v, bf16x2_t)); }
;     __device__ __forceinline__ void operator()(Acc& acc, const GUnit& u, int wr, int wc, int fr, int fq, LAS unsigned char* xl, int wid, int lane) const {
;     ...
;             for (int m = 0; m < 4; ++m) { const int rl = ai * HALF + wr * 64 + m * 16 + fr; const f32x2 st = tab[rl];
;                 bf16_t* rowp = H + (size_t)(row0 + ai * HALF + m * 16) * 512 + col0;
;                 float h[8];
; #pragma unroll
;                 for (int nn = 0; nn < 2; ++nn) { const f32x4 g0 = *(const LAS f32x4*)(Gl + cl + 4 * nn), g1 = *(const LAS f32x4*)(Gl + HALF + cl + 4 * nn), b0 = *(const LAS f32x4*)(Bl + cl + 4 * nn), b1 = *(const LAS f32x4*)(Bl + HALF + cl + 4 * nn);
;                     const f32x4 a4 = (acc[ai][0][m][nn] - g0 * st.x) * st.y + b0, b4 = (acc[ai][1][m][nn] - g1 * st.x) * st.y + b1;
; #pragma unroll
;                     for (int jj = 0; jj < 4; ++jj) { const float a = a4[jj], b = b4[jj]; h[nn * 4 + jj] = a * b * __builtin_amdgcn_rcpf(1.0f + __builtin_amdgcn_exp2f(-a * 1.4426950408889634f)); } }
;                 u32x4 w; w.x = cvt_pk_bf16(h[0], h[1]); w.y = cvt_pk_bf16(h[2], h[3]); w.z = cvt_pk_bf16(h[4], h[5]); w.w = cvt_pk_bf16(h[6], h[7]);
;                 *(u32x4*)rowp = w; __builtin_amdgcn_sched_barrier(0); }
	v_pk_fma_f32 v[50:51], v[86:87], v[54:55], v[50:51] op_sel_hi:[0,1,1] neg_lo:[1,0,0] neg_hi:[1,0,0]
	v_pk_fma_f32 v[50:51], v[86:87], v[50:51], v[58:59] op_sel:[1,0,0]
	ds_read_b128 v[74:77], v226 offset:16
	ds_read_b128 v[78:81], v227
	ds_read_b128 v[82:85], v227 offset:16
	v_mul_f32_e32 v2, 0xbfb8aa3b, v50
	v_exp_f32_e32 v2, v2
	v_pk_fma_f32 v[46:47], v[86:87], v[70:71], v[46:47] op_sel_hi:[0,1,1] neg_lo:[1,0,0] neg_hi:[1,0,0]
	s_waitcnt lgkmcnt(0)
	v_pk_fma_f32 v[46:47], v[86:87], v[46:47], v[78:79] op_sel:[1,0,0]
	v_pk_fma_f32 v[42:43], v[86:87], v[66:67], v[42:43] op_sel_hi:[0,1,1] neg_lo:[1,0,0] neg_hi:[1,0,0]
	v_add_f32_e32 v2, 1.0, v2
	v_rcp_f32_e32 v54, v2
	v_mul_f32_e32 v2, 0xbfb8aa3b, v51
	v_exp_f32_e32 v2, v2
	v_pk_mul_f32 v[46:47], v[50:51], v[46:47]
	v_pk_fma_f32 v[50:51], v[86:87], v[56:57], v[52:53] op_sel_hi:[0,1,1] neg_lo:[1,0,0] neg_hi:[1,0,0]
	v_pk_fma_f32 v[50:51], v[86:87], v[50:51], v[60:61] op_sel:[1,0,0]
	v_add_f32_e32 v2, 1.0, v2
	v_rcp_f32_e32 v55, v2
	v_mul_f32_e32 v2, 0xbfb8aa3b, v50
	v_exp_f32_e32 v2, v2
	v_mul_f32_e32 v52, 0xbfb8aa3b, v51
	v_exp_f32_e32 v53, v52
	v_pk_fma_f32 v[42:43], v[86:87], v[42:43], v[74:75] op_sel:[1,0,0]
	v_add_f32_e32 v2, 1.0, v2
	v_rcp_f32_e32 v52, v2
	v_add_f32_e32 v2, 1.0, v53
	v_rcp_f32_e32 v53, v2
	v_mul_f32_e32 v2, 0xbfb8aa3b, v42
	v_exp_f32_e32 v2, v2
	v_pk_fma_f32 v[48:49], v[86:87], v[72:73], v[48:49] op_sel_hi:[0,1,1] neg_lo:[1,0,0] neg_hi:[1,0,0]
	v_pk_fma_f32 v[48:49], v[86:87], v[48:49], v[80:81] op_sel:[1,0,0]
	v_pk_fma_f32 v[38:39], v[86:87], v[62:63], v[38:39] op_sel_hi:[0,1,1] neg_lo:[1,0,0] neg_hi:[1,0,0]
	v_add_f32_e32 v2, 1.0, v2
	v_pk_mul_f32 v[48:49], v[50:51], v[48:49]
	v_rcp_f32_e32 v50, v2
	v_mul_f32_e32 v2, 0xbfb8aa3b, v43
	v_exp_f32_e32 v2, v2
	v_pk_fma_f32 v[38:39], v[86:87], v[38:39], v[82:83] op_sel:[1,0,0]
	v_pk_mul_f32 v[48:49], v[48:49], v[52:53]
	v_pk_mul_f32 v[38:39], v[42:43], v[38:39]
	v_pk_fma_f32 v[42:43], v[86:87], v[68:69], v[44:45] op_sel_hi:[0,1,1] neg_lo:[1,0,0] neg_hi:[1,0,0]
	v_add_f32_e32 v2, 1.0, v2
	v_pk_fma_f32 v[42:43], v[86:87], v[42:43], v[76:77] op_sel:[1,0,0]
	v_rcp_f32_e32 v51, v2
	v_mul_f32_e32 v2, 0xbfb8aa3b, v42
	v_exp_f32_e32 v2, v2
	v_mul_f32_e32 v44, 0xbfb8aa3b, v43
	v_exp_f32_e32 v52, v44
	v_pk_mul_f32 v[44:45], v[38:39], v[50:51]
	v_add_f32_e32 v2, 1.0, v2
	v_rcp_f32_e32 v38, v2
	v_add_f32_e32 v2, 1.0, v52
	v_rcp_f32_e32 v39, v2
	v_pk_fma_f32 v[40:41], v[86:87], v[64:65], v[40:41] op_sel_hi:[0,1,1] neg_lo:[1,0,0] neg_hi:[1,0,0]
	v_pk_fma_f32 v[40:41], v[86:87], v[40:41], v[84:85] op_sel:[1,0,0]
	v_pk_mul_f32 v[46:47], v[46:47], v[54:55]
	v_pk_mul_f32 v[40:41], v[42:43], v[40:41]
	s_nop 0
	v_pk_mul_f32 v[42:43], v[40:41], v[38:39]
	v_cvt_pk_bf16_f32 v38, v46, v47
	v_cvt_pk_bf16_f32 v41, v42, v43
	v_add_co_u32_e32 v42, vcc, s48, v4
	v_cvt_pk_bf16_f32 v39, v48, v49
	v_cvt_pk_bf16_f32 v40, v44, v45
	v_addc_co_u32_e32 v43, vcc, 0, v5, vcc
	global_store_dwordx4 v[42:43], v[38:41], off
	ds_read_b64 v[70:71], v223 offset:1280
	ds_read_b128 v[38:41], v224
	ds_read_b128 v[42:45], v226
	ds_read_b128 v[46:49], v225 offset:16
	ds_read_b128 v[50:53], v224 offset:16
	ds_read_b128 v[54:57], v225
	s_waitcnt lgkmcnt(0)
	v_pk_fma_f32 v[34:35], v[70:71], v[38:39], v[34:35] op_sel_hi:[0,1,1] neg_lo:[1,0,0] neg_hi:[1,0,0]
	v_pk_fma_f32 v[34:35], v[70:71], v[34:35], v[42:43] op_sel:[1,0,0]
	ds_read_b128 v[58:61], v226 offset:16
	ds_read_b128 v[62:65], v227
	ds_read_b128 v[66:69], v227 offset:16
	v_mul_f32_e32 v2, 0xbfb8aa3b, v34
	v_exp_f32_e32 v2, v2
	v_pk_fma_f32 v[30:31], v[70:71], v[54:55], v[30:31] op_sel_hi:[0,1,1] neg_lo:[1,0,0] neg_hi:[1,0,0]
	s_waitcnt lgkmcnt(0)
; #define LAS __attribute__((address_space(3)))
; #define PG8_BAR __builtin_amdgcn_s_barrier()
; template <class Epi, class Sched, bool GATHER, bool LIGHTSKIP = false>
; __device__ __forceinline__ void gemm_phase(LAS unsigned char* lds, LAS unsigned char* xl, const int lda, const int ldb, const int K, const Sched& S, const Epi& E) {
;     ...
;         if (wr == 0) PG8_BAR;
;         E(acc, cur, wr, wc, fr, fq, xl, wid, lane);
;         if (!has_next) break;
; #pragma unroll
;         for (int a = 0; a < 2; ++a)
; #pragma unroll
;             for (int b = 0; b < 2; ++b)
; #pragma unroll
;                 for (int m = 0; m < 4; ++m)
; #pragma unroll
;                     for (int n = 0; n < 2; ++n) acc[a][b][m][n] = (f32x4){0.f, 0.f, 0.f, 0.f};
;         cur = nxt; cA = nA; cB = nB; ++ui;
;         if constexpr (GATHER) {
; #pragma unroll
;             for (int h = 0; h < 2; ++h) { vc[h][0] = vn[h][0]; vc[h][1] = vn[h][1]; } }
;         if (wr == 1) PG8_BAR;
;     __device__ __forceinline__ void operator()(Acc& acc, const GUnit& u, int wr, int wc, int fr, int fq, LAS unsigned char* xl, int wid, int lane) const {
;     ...
;             for (int m = 0; m < 4; ++m) { const int rl = ai * HALF + wr * 64 + m * 16 + fr; const f32x2 st = tab[rl];
;                 bf16_t* rowp = H + (size_t)(row0 + ai * HALF + m * 16) * 512 + col0;
;                 float h[8];
; #pragma unroll
;                 for (int nn = 0; nn < 2; ++nn) { const f32x4 g0 = *(const LAS f32x4*)(Gl + cl + 4 * nn), g1 = *(const LAS f32x4*)(Gl + HALF + cl + 4 * nn), b0 = *(const LAS f32x4*)(Bl + cl + 4 * nn), b1 = *(const LAS f32x4*)(Bl + HALF + cl + 4 * nn);
;                     const f32x4 a4 = (acc[ai][0][m][nn] - g0 * st.x) * st.y + b0, b4 = (acc[ai][1][m][nn] - g1 * st.x) * st.y + b1;
; #pragma unroll
;                     for (int jj = 0; jj < 4; ++jj) { const float a = a4[jj], b = b4[jj]; h[nn * 4 + jj] = a * b * __builtin_amdgcn_rcpf(1.0f + __builtin_amdgcn_exp2f(-a * 1.4426950408889634f)); } }
;                 u32x4 w; w.x = cvt_pk_bf16(h[0], h[1]); w.y = cvt_pk_bf16(h[2], h[3]); w.z = cvt_pk_bf16(h[4], h[5]); w.w = cvt_pk_bf16(h[6], h[7]);
;                 *(u32x4*)rowp = w; __builtin_amdgcn_sched_barrier(0); }
;         asm volatile("s_waitcnt lgkmcnt(0)" ::: "memory"); __builtin_amdgcn_s_barrier(); asm volatile("" ::: "memory");
	v_pk_fma_f32 v[30:31], v[70:71], v[30:31], v[62:63] op_sel:[1,0,0]
	v_pk_fma_f32 v[26:27], v[70:71], v[50:51], v[26:27] op_sel_hi:[0,1,1] neg_lo:[1,0,0] neg_hi:[1,0,0]
	v_add_f32_e32 v2, 1.0, v2
	v_rcp_f32_e32 v38, v2
	v_mul_f32_e32 v2, 0xbfb8aa3b, v35
	v_exp_f32_e32 v2, v2
	v_pk_mul_f32 v[30:31], v[34:35], v[30:31]
	v_pk_fma_f32 v[34:35], v[70:71], v[40:41], v[36:37] op_sel_hi:[0,1,1] neg_lo:[1,0,0] neg_hi:[1,0,0]
	v_pk_fma_f32 v[34:35], v[70:71], v[34:35], v[44:45] op_sel:[1,0,0]
	v_add_f32_e32 v2, 1.0, v2
	v_rcp_f32_e32 v39, v2
	v_mul_f32_e32 v2, 0xbfb8aa3b, v34
	v_exp_f32_e32 v2, v2
	v_mul_f32_e32 v36, 0xbfb8aa3b, v35
	v_exp_f32_e32 v37, v36
	v_pk_fma_f32 v[26:27], v[70:71], v[26:27], v[58:59] op_sel:[1,0,0]
	v_add_f32_e32 v2, 1.0, v2
	v_rcp_f32_e32 v36, v2
	v_add_f32_e32 v2, 1.0, v37
	v_rcp_f32_e32 v37, v2
	v_mul_f32_e32 v2, 0xbfb8aa3b, v26
	v_exp_f32_e32 v2, v2
	v_pk_fma_f32 v[32:33], v[70:71], v[56:57], v[32:33] op_sel_hi:[0,1,1] neg_lo:[1,0,0] neg_hi:[1,0,0]
	v_pk_fma_f32 v[32:33], v[70:71], v[32:33], v[64:65] op_sel:[1,0,0]
	v_pk_fma_f32 v[22:23], v[70:71], v[46:47], v[22:23] op_sel_hi:[0,1,1] neg_lo:[1,0,0] neg_hi:[1,0,0]
	v_add_f32_e32 v2, 1.0, v2
	v_pk_mul_f32 v[32:33], v[34:35], v[32:33]
	v_rcp_f32_e32 v34, v2
	v_mul_f32_e32 v2, 0xbfb8aa3b, v27
	v_exp_f32_e32 v2, v2
	v_pk_fma_f32 v[22:23], v[70:71], v[22:23], v[66:67] op_sel:[1,0,0]
	v_pk_mul_f32 v[32:33], v[32:33], v[36:37]
	v_pk_mul_f32 v[22:23], v[26:27], v[22:23]
	v_pk_fma_f32 v[26:27], v[70:71], v[52:53], v[28:29] op_sel_hi:[0,1,1] neg_lo:[1,0,0] neg_hi:[1,0,0]
	v_add_f32_e32 v2, 1.0, v2
	v_pk_fma_f32 v[26:27], v[70:71], v[26:27], v[60:61] op_sel:[1,0,0]
	v_rcp_f32_e32 v35, v2
	v_mul_f32_e32 v2, 0xbfb8aa3b, v26
	v_exp_f32_e32 v2, v2
	v_mul_f32_e32 v28, 0xbfb8aa3b, v27
	v_exp_f32_e32 v36, v28
	v_pk_mul_f32 v[28:29], v[22:23], v[34:35]
	v_add_f32_e32 v2, 1.0, v2
	v_rcp_f32_e32 v22, v2
	v_add_f32_e32 v2, 1.0, v36
	v_rcp_f32_e32 v23, v2
	v_pk_fma_f32 v[24:25], v[70:71], v[48:49], v[24:25] op_sel_hi:[0,1,1] neg_lo:[1,0,0] neg_hi:[1,0,0]
	v_pk_fma_f32 v[24:25], v[70:71], v[24:25], v[68:69] op_sel:[1,0,0]
	v_pk_mul_f32 v[30:31], v[30:31], v[38:39]
	v_pk_mul_f32 v[24:25], v[26:27], v[24:25]
	s_nop 0
	v_pk_mul_f32 v[26:27], v[24:25], v[22:23]
	v_cvt_pk_bf16_f32 v22, v30, v31
	v_cvt_pk_bf16_f32 v25, v26, v27
	v_add_co_u32_e32 v26, vcc, s49, v4
	v_cvt_pk_bf16_f32 v23, v32, v33
	v_cvt_pk_bf16_f32 v24, v28, v29
	v_addc_co_u32_e32 v27, vcc, 0, v5, vcc
	global_store_dwordx4 v[26:27], v[22:25], off
	ds_read_b64 v[54:55], v223 offset:1408
	ds_read_b128 v[22:25], v224
	ds_read_b128 v[26:29], v226
	ds_read_b128 v[30:33], v225 offset:16
	ds_read_b128 v[34:37], v224 offset:16
	ds_read_b128 v[38:41], v225
	s_waitcnt lgkmcnt(0)
	v_pk_fma_f32 v[18:19], v[54:55], v[22:23], v[18:19] op_sel_hi:[0,1,1] neg_lo:[1,0,0] neg_hi:[1,0,0]
	v_pk_fma_f32 v[18:19], v[54:55], v[18:19], v[26:27] op_sel:[1,0,0]
	ds_read_b128 v[42:45], v226 offset:16
	ds_read_b128 v[46:49], v227
	ds_read_b128 v[50:53], v227 offset:16
	v_mul_f32_e32 v2, 0xbfb8aa3b, v18
	v_exp_f32_e32 v2, v2
	v_pk_fma_f32 v[14:15], v[54:55], v[38:39], v[14:15] op_sel_hi:[0,1,1] neg_lo:[1,0,0] neg_hi:[1,0,0]
	s_waitcnt lgkmcnt(0)
	v_pk_fma_f32 v[14:15], v[54:55], v[14:15], v[46:47] op_sel:[1,0,0]
	v_pk_fma_f32 v[10:11], v[54:55], v[34:35], v[10:11] op_sel_hi:[0,1,1] neg_lo:[1,0,0] neg_hi:[1,0,0]
	v_add_f32_e32 v2, 1.0, v2
	v_rcp_f32_e32 v22, v2
	v_mul_f32_e32 v2, 0xbfb8aa3b, v19
	v_exp_f32_e32 v2, v2
	v_pk_mul_f32 v[14:15], v[18:19], v[14:15]
	v_pk_fma_f32 v[18:19], v[54:55], v[24:25], v[20:21] op_sel_hi:[0,1,1] neg_lo:[1,0,0] neg_hi:[1,0,0]
	v_pk_fma_f32 v[18:19], v[54:55], v[18:19], v[28:29] op_sel:[1,0,0]
	v_add_f32_e32 v2, 1.0, v2
	v_rcp_f32_e32 v23, v2
	v_mul_f32_e32 v2, 0xbfb8aa3b, v18
	v_exp_f32_e32 v2, v2
	v_mul_f32_e32 v20, 0xbfb8aa3b, v19
	v_exp_f32_e32 v21, v20
	v_pk_fma_f32 v[10:11], v[54:55], v[10:11], v[42:43] op_sel:[1,0,0]
	v_add_f32_e32 v2, 1.0, v2
	v_rcp_f32_e32 v20, v2
	v_add_f32_e32 v2, 1.0, v21
	v_rcp_f32_e32 v21, v2
	v_mul_f32_e32 v2, 0xbfb8aa3b, v10
	v_exp_f32_e32 v2, v2
	v_pk_fma_f32 v[16:17], v[54:55], v[40:41], v[16:17] op_sel_hi:[0,1,1] neg_lo:[1,0,0] neg_hi:[1,0,0]
	v_pk_fma_f32 v[16:17], v[54:55], v[16:17], v[48:49] op_sel:[1,0,0]
	v_pk_fma_f32 v[6:7], v[54:55], v[30:31], v[6:7] op_sel_hi:[0,1,1] neg_lo:[1,0,0] neg_hi:[1,0,0]
	v_add_f32_e32 v2, 1.0, v2
	v_pk_mul_f32 v[16:17], v[18:19], v[16:17]
	v_rcp_f32_e32 v18, v2
	v_mul_f32_e32 v2, 0xbfb8aa3b, v11
	v_exp_f32_e32 v2, v2
	v_pk_fma_f32 v[6:7], v[54:55], v[6:7], v[50:51] op_sel:[1,0,0]
	v_pk_mul_f32 v[16:17], v[16:17], v[20:21]
	v_pk_mul_f32 v[6:7], v[10:11], v[6:7]
	v_pk_fma_f32 v[10:11], v[54:55], v[36:37], v[12:13] op_sel_hi:[0,1,1] neg_lo:[1,0,0] neg_hi:[1,0,0]
	v_add_f32_e32 v2, 1.0, v2
	v_pk_fma_f32 v[10:11], v[54:55], v[10:11], v[44:45] op_sel:[1,0,0]
	v_rcp_f32_e32 v19, v2
	v_mul_f32_e32 v2, 0xbfb8aa3b, v10
	v_exp_f32_e32 v2, v2
	v_mul_f32_e32 v12, 0xbfb8aa3b, v11
	v_exp_f32_e32 v20, v12
	v_pk_mul_f32 v[12:13], v[6:7], v[18:19]
	v_add_f32_e32 v2, 1.0, v2
	v_rcp_f32_e32 v6, v2
	v_add_f32_e32 v2, 1.0, v20
	v_rcp_f32_e32 v7, v2
	v_pk_fma_f32 v[8:9], v[54:55], v[32:33], v[8:9] op_sel_hi:[0,1,1] neg_lo:[1,0,0] neg_hi:[1,0,0]
	v_pk_fma_f32 v[8:9], v[54:55], v[8:9], v[52:53] op_sel:[1,0,0]
	v_pk_mul_f32 v[14:15], v[14:15], v[22:23]
	v_pk_mul_f32 v[8:9], v[10:11], v[8:9]
	v_add_co_u32_e32 v4, vcc, 0x2c000, v4
	v_pk_mul_f32 v[10:11], v[8:9], v[6:7]
	v_cvt_pk_bf16_f32 v6, v14, v15
	v_cvt_pk_bf16_f32 v7, v16, v17
	v_cvt_pk_bf16_f32 v8, v12, v13
	v_cvt_pk_bf16_f32 v9, v10, v11
	v_addc_co_u32_e32 v5, vcc, 0, v5, vcc
	global_store_dwordx4 v[4:5], v[6:9], off
	s_waitcnt lgkmcnt(0)
	s_barrier
	s_andn2_b64 vcc, exec, s[22:23]
	s_mov_b64 s[6:7], -1
	s_cbranch_vccnz .LBB0_1334
	s_andn2_b64 vcc, exec, s[10:11]
	s_cbranch_vccnz .LBB0_1333
	s_barrier
	s_branch .LBB0_1333
